# baseline (speedup 1.0000x reference)
_Z7kfinal3PKDF16_PKfS2_S2_PK15HIP_vector_typeIjLj4EES2_Pf:
	s_load_dwordx2 s[20:21], s[0:1], 0x20
	s_lshl_b32 s43, s2, 1
	s_and_b32 s43, s43, 64
	s_lshl_b32 s44, s2, 2
	s_and_b32 s44, s44, 28
	s_lshr_b32 s45, s2, 6
	s_add_i32 s44, s44, s45
	s_lshl_b32 s44, s44, 2
	s_add_i32 s44, s44, -1
	v_and_b32_e32 v136, 63, v0
	v_lshrrev_b32_e32 v137, 6, v0
	v_or_b32_e32 v138, 8, v137
	v_or_b32_e32 v139, 16, v137
	s_movk_i32 s38, 0xff94
	s_movk_i32 s39, 0xffee
	s_add_i32 s40, s43, -4
	v_mov_b32_e32 v131, 0x7f
	v_mov_b32_e32 v132, 0x7c
	v_min_u32_e32 v133, 27, v139
	v_min_u32_e32 v134, 3, v137
	v_or_b32_e32 v134, 24, v134
	v_lshl_or_b32 v128, v137, 6, v136
	v_mul_u32_u24_e32 v129, 0x25f, v128
	v_lshrrev_b32_e32 v129, 16, v129
	v_mad_i32_i24 v128, v129, s38, v128
	v_mul_u32_u24_e32 v130, 0xe39, v128
	v_lshrrev_b32_e32 v130, 16, v130
	v_mad_i32_i24 v128, v130, s39, v128
	v_add_u32_e32 v130, s44, v130
	v_med3_i32 v130, v130, 0, v131
	v_lshl_add_u32 v128, v128, 2, s40
	v_med3_i32 v128, v128, 0, v132
	v_min_u32_e32 v129, 15, v129
	v_lshlrev_b32_e32 v129, 14, v129
	v_lshlrev_b32_e32 v130, 7, v130
	v_or3_b32 v94, v130, v129, v128
	v_lshl_or_b32 v128, v138, 6, v136
	v_mul_u32_u24_e32 v129, 0x25f, v128
	v_lshrrev_b32_e32 v129, 16, v129
	v_mad_i32_i24 v128, v129, s38, v128
	v_mul_u32_u24_e32 v130, 0xe39, v128
	v_lshrrev_b32_e32 v130, 16, v130
	v_mad_i32_i24 v128, v130, s39, v128
	v_add_u32_e32 v130, s44, v130
	v_med3_i32 v130, v130, 0, v131
	v_lshl_add_u32 v128, v128, 2, s40
	v_med3_i32 v128, v128, 0, v132
	v_min_u32_e32 v129, 15, v129
	v_lshlrev_b32_e32 v129, 14, v129
	v_lshlrev_b32_e32 v130, 7, v130
	v_or3_b32 v96, v130, v129, v128
	v_lshl_or_b32 v128, v133, 6, v136
	v_mul_u32_u24_e32 v129, 0x25f, v128
	v_lshrrev_b32_e32 v129, 16, v129
	v_mad_i32_i24 v128, v129, s38, v128
	v_mul_u32_u24_e32 v130, 0xe39, v128
	v_lshrrev_b32_e32 v130, 16, v130
	v_mad_i32_i24 v128, v130, s39, v128
	v_add_u32_e32 v130, s44, v130
	v_med3_i32 v130, v130, 0, v131
	v_lshl_add_u32 v128, v128, 2, s40
	v_med3_i32 v128, v128, 0, v132
	v_min_u32_e32 v129, 15, v129
	v_lshlrev_b32_e32 v129, 14, v129
	v_lshlrev_b32_e32 v130, 7, v130
	v_or3_b32 v98, v130, v129, v128
	v_lshl_or_b32 v128, v134, 6, v136
	v_mul_u32_u24_e32 v129, 0x25f, v128
	v_lshrrev_b32_e32 v129, 16, v129
	v_mad_i32_i24 v128, v129, s38, v128
	v_mul_u32_u24_e32 v130, 0xe39, v128
	v_lshrrev_b32_e32 v130, 16, v130
	v_mad_i32_i24 v128, v130, s39, v128
	v_add_u32_e32 v130, s44, v130
	v_med3_i32 v130, v130, 0, v131
	v_lshl_add_u32 v128, v128, 2, s40
	v_med3_i32 v128, v128, 0, v132
	v_min_u32_e32 v129, 15, v129
	v_lshlrev_b32_e32 v129, 14, v129
	v_lshlrev_b32_e32 v130, 7, v130
	v_or3_b32 v100, v130, v129, v128
	v_cmp_eq_u32_e32 vcc, 27, v134
	v_readfirstlane_b32 s41, v100
	s_nop 1
	v_mov_b32_e32 v135, s41
	v_cndmask_b32_e32 v100, v100, v135, vcc
	v_accvgpr_write_b32 a3, 0
	v_accvgpr_write_b32 a2, 0
	v_accvgpr_write_b32 a1, 0
	v_accvgpr_write_b32 a0, 0
	v_accvgpr_write_b32 a7, 0
	v_accvgpr_write_b32 a6, 0
	v_accvgpr_write_b32 a5, 0
	v_accvgpr_write_b32 a4, 0
	v_accvgpr_write_b32 a15, 0
	v_accvgpr_write_b32 a14, 0
	v_accvgpr_write_b32 a13, 0
	v_accvgpr_write_b32 a12, 0
	v_accvgpr_write_b32 a19, 0
	v_accvgpr_write_b32 a18, 0
	v_accvgpr_write_b32 a17, 0
	v_accvgpr_write_b32 a16, 0
	v_accvgpr_write_b32 a31, 0
	v_accvgpr_write_b32 a30, 0
	v_accvgpr_write_b32 a29, 0
	v_accvgpr_write_b32 a28, 0
	v_accvgpr_write_b32 a63, 0
	v_accvgpr_write_b32 a62, 0
	v_accvgpr_write_b32 a61, 0
	v_accvgpr_write_b32 a60, 0
	v_accvgpr_write_b32 a11, 0
	v_accvgpr_write_b32 a10, 0
	v_accvgpr_write_b32 a9, 0
	v_accvgpr_write_b32 a8, 0
	v_accvgpr_write_b32 a23, 0
	v_accvgpr_write_b32 a22, 0
	v_accvgpr_write_b32 a21, 0
	v_accvgpr_write_b32 a20, 0
	v_accvgpr_write_b32 a27, 0
	v_accvgpr_write_b32 a26, 0
	v_accvgpr_write_b32 a25, 0
	v_accvgpr_write_b32 a24, 0
	v_accvgpr_write_b32 a39, 0
	v_accvgpr_write_b32 a38, 0
	v_accvgpr_write_b32 a37, 0
	v_accvgpr_write_b32 a36, 0
	v_accvgpr_write_b32 a47, 0
	v_accvgpr_write_b32 a46, 0
	v_accvgpr_write_b32 a45, 0
	v_accvgpr_write_b32 a44, 0
	v_accvgpr_write_b32 a67, 0
	v_accvgpr_write_b32 a66, 0
	v_accvgpr_write_b32 a65, 0
	v_accvgpr_write_b32 a64, 0
	v_accvgpr_write_b32 a35, 0
	v_accvgpr_write_b32 a34, 0
	v_accvgpr_write_b32 a33, 0
	v_accvgpr_write_b32 a32, 0
	v_accvgpr_write_b32 a43, 0
	v_accvgpr_write_b32 a42, 0
	v_accvgpr_write_b32 a41, 0
	v_accvgpr_write_b32 a40, 0
	v_accvgpr_write_b32 a51, 0
	v_accvgpr_write_b32 a50, 0
	v_accvgpr_write_b32 a49, 0
	v_accvgpr_write_b32 a48, 0
	v_accvgpr_write_b32 a55, 0
	v_accvgpr_write_b32 a54, 0
	v_accvgpr_write_b32 a53, 0
	v_accvgpr_write_b32 a52, 0
	v_accvgpr_write_b32 a59, 0
	v_accvgpr_write_b32 a58, 0
	v_accvgpr_write_b32 a57, 0
	v_accvgpr_write_b32 a56, 0
	v_accvgpr_write_b32 a71, 0
	v_accvgpr_write_b32 a70, 0
	v_accvgpr_write_b32 a69, 0
	v_accvgpr_write_b32 a68, 0
	v_lshrrev_b32_e32 v48, 6, v0
	s_bfe_u32 s24, s2, 0x20003
	s_mul_i32 s3, s24, 0x28800
	v_lshlrev_b32_e32 v118, 10, v48
	v_and_b32_e32 v1, 63, v0
	s_waitcnt lgkmcnt(0)
	s_add_u32 s6, s20, s3
	v_add_u32_e32 v2, 0, v118
	s_addc_u32 s7, s21, 0
	v_mov_b32_e32 v47, 0
	v_lshlrev_b32_e32 v46, 4, v1
	v_accvgpr_write_b32 a72, v2
	v_add_u32_e32 v8, 0xc600, v2
	v_and_b32_e32 v2, 0x1c0, v0
	v_lshl_add_u64 v[4:5], s[6:7], 0, v[46:47]
	v_lshlrev_b32_e32 v2, 4, v2
	v_mov_b32_e32 v3, v47
	v_readfirstlane_b32 s3, v8
	v_lshl_add_u64 v[6:7], v[4:5], 0, v[2:3]
	s_mov_b32 m0, s3
	v_or_b32_e32 v49, 8, v48
	global_load_lds_dwordx4 v[6:7], off
	s_movk_i32 s3, 0x280
	v_cmp_gt_u32_e64 s[4:5], s3, v0
	v_lshlrev_b32_e32 v90, 10, v49
	s_and_saveexec_b64 s[8:9], s[4:5]
	s_cbranch_execz .LBB3_2
	v_add_u32_e32 v3, 0, v90
	v_add_u32_e32 v3, 0xc600, v3
	v_mov_b32_e32 v91, v47
	v_readfirstlane_b32 s3, v3
	v_lshl_add_u64 v[6:7], v[4:5], 0, v[90:91]
	s_mov_b32 m0, s3
	s_nop 0
	global_load_lds_dwordx4 v[6:7], off

.Lk3_h2:
	v_mfma_f32_16x16x32_f16 a[0:3], v[70:73], v[82:85], a[0:3]
	ds_read_b128 v[14:17], v126
	v_mfma_f32_16x16x32_f16 a[4:7], v[70:73], v[86:89], a[4:7]
	ds_read_b128 v[18:21], v127
	v_mfma_f32_16x16x32_f16 a[12:15], v[66:69], v[82:85], a[12:15]
	ds_read_b128 v[42:45], v131
	v_mfma_f32_16x16x32_f16 a[16:19], v[66:69], v[86:89], a[16:19]
	ds_read_b128 v[38:41], v131 offset:1024
	v_mfma_f32_16x16x32_f16 a[28:31], v[58:61], v[82:85], a[28:31]
	ds_read_b128 v[34:37], v131 offset:2048
	v_mfma_f32_16x16x32_f16 a[60:63], v[58:61], v[86:89], a[60:63]
	ds_read_b128 v[30:33], v131 offset:3072
	v_mfma_f32_16x16x32_f16 a[8:11], v[54:57], v[82:85], a[8:11]
	ds_read_b128 v[26:29], v131 offset:4096
	v_mfma_f32_16x16x32_f16 a[20:23], v[54:57], v[86:89], a[20:23]
	ds_read_b128 v[22:25], v131 offset:5120
	v_mfma_f32_16x16x32_f16 a[24:27], v[46:49], v[82:85], a[24:27]
	ds_read_b128 v[10:13], v131 offset:6144
	v_mfma_f32_16x16x32_f16 a[36:39], v[46:49], v[86:89], a[36:39]
	ds_read_b128 v[6:9], v131 offset:7168
	v_mfma_f32_16x16x32_f16 a[44:47], v[50:53], v[82:85], a[44:47]
	ds_read_b128 v[2:5], v131 offset:8192
	v_mfma_f32_16x16x32_f16 a[64:67], v[50:53], v[86:89], a[64:67]
	v_mfma_f32_16x16x32_f16 a[32:35], v[62:65], v[82:85], a[32:35]
	v_mfma_f32_16x16x32_f16 a[40:43], v[62:65], v[86:89], a[40:43]
	v_mfma_f32_16x16x32_f16 a[48:51], v[74:77], v[82:85], a[48:51]
	v_mfma_f32_16x16x32_f16 a[52:55], v[74:77], v[86:89], a[52:55]
	v_mfma_f32_16x16x32_f16 a[56:59], v[78:81], v[82:85], a[56:59]
	v_mfma_f32_16x16x32_f16 a[68:71], v[78:81], v[86:89], a[68:71]
	v_lshl_add_u64 v[116:117], v[116:117], 0, s[6:7]
	s_mov_b32 s19, s15
	s_cmp_eq_u32 s15, 9
	s_cbranch_scc0 .Lk3_top
	s_waitcnt lgkmcnt(0)
	s_setprio 0

	.amdhsa_kernel _Z7kfinal3PKDF16_PKfS2_S2_PK15HIP_vector_typeIjLj4EES2_Pf
		.amdhsa_group_segment_fixed_size 0
		.amdhsa_private_segment_fixed_size 0
		.amdhsa_kernarg_size 56
		.amdhsa_user_sgpr_count 2
		.amdhsa_user_sgpr_dispatch_ptr 0
		.amdhsa_user_sgpr_queue_ptr 0
		.amdhsa_user_sgpr_kernarg_segment_ptr 1
		.amdhsa_user_sgpr_dispatch_id 0
		.amdhsa_user_sgpr_kernarg_preload_length 0
		.amdhsa_user_sgpr_kernarg_preload_offset 0
		.amdhsa_user_sgpr_private_segment_size 0
		.amdhsa_uses_dynamic_stack 0
		.amdhsa_enable_private_segment 0
		.amdhsa_system_sgpr_workgroup_id_x 1
		.amdhsa_system_sgpr_workgroup_id_y 0
		.amdhsa_system_sgpr_workgroup_id_z 0
		.amdhsa_system_sgpr_workgroup_info 0
		.amdhsa_system_vgpr_workitem_id 0
		.amdhsa_next_free_vgpr 213
		.amdhsa_next_free_sgpr 46
		.amdhsa_accum_offset 140
		.amdhsa_reserve_vcc 1
		.amdhsa_float_round_mode_32 0
		.amdhsa_float_round_mode_16_64 0
		.amdhsa_float_denorm_mode_32 3
		.amdhsa_float_denorm_mode_16_64 3
		.amdhsa_dx10_clamp 1
		.amdhsa_ieee_mode 1
		.amdhsa_fp16_overflow 0
		.amdhsa_tg_split 0
		.amdhsa_exception_fp_ieee_invalid_op 0
		.amdhsa_exception_fp_denorm_src 0
		.amdhsa_exception_fp_ieee_div_zero 0
		.amdhsa_exception_fp_ieee_overflow 0
		.amdhsa_exception_fp_ieee_underflow 0
		.amdhsa_exception_fp_ieee_inexact 0
		.amdhsa_exception_int_div_zero 0
	.end_amdhsa_kernel

amdhsa.kernels:
  - .agpr_count:     0
    .args:
      - .actual_access:  read_only
        .address_space:  global
        .offset:         0
        .size:           8
        .value_kind:     global_buffer
      - .actual_access:  read_only
        .address_space:  global
        .offset:         8
        .size:           8
        .value_kind:     global_buffer
      - .actual_access:  read_only
        .address_space:  global
        .offset:         16
        .size:           8
        .value_kind:     global_buffer
      - .actual_access:  read_only
        .address_space:  global
        .offset:         24
        .size:           8
        .value_kind:     global_buffer
      - .actual_access:  read_only
        .address_space:  global
        .offset:         32
        .size:           8
        .value_kind:     global_buffer
      - .actual_access:  read_only
        .address_space:  global
        .offset:         40
        .size:           8
        .value_kind:     global_buffer
      - .actual_access:  write_only
        .address_space:  global
        .offset:         48
        .size:           8
        .value_kind:     global_buffer
      - .actual_access:  write_only
        .address_space:  global
        .offset:         56
        .size:           8
        .value_kind:     global_buffer
      - .actual_access:  write_only
        .address_space:  global
        .offset:         64
        .size:           8
        .value_kind:     global_buffer
      - .actual_access:  write_only
        .address_space:  global
        .offset:         72
        .size:           8
        .value_kind:     global_buffer
    .group_segment_fixed_size: 12000
    .kernarg_segment_align: 8
    .kernarg_segment_size: 80
    .language:       OpenCL C
    .language_version:
      - 2
      - 0
    .max_flat_workgroup_size: 256
    .name:           _Z2k0PKfS0_S0_S0_S0_S0_PDF16_PfS1_S1_
    .private_segment_fixed_size: 0
    .sgpr_count:     24
    .sgpr_spill_count: 0
    .symbol:         _Z2k0PKfS0_S0_S0_S0_S0_PDF16_PfS1_S1_.kd
    .uniform_work_group_size: 1
    .uses_dynamic_stack: false
    .vgpr_count:     150
    .vgpr_spill_count: 0
    .wavefront_size: 64
  - .agpr_count:     16
    .args:
      - .actual_access:  read_only
        .address_space:  global
        .offset:         0
        .size:           8
        .value_kind:     global_buffer
      - .actual_access:  read_only
        .address_space:  global
        .offset:         8
        .size:           8
        .value_kind:     global_buffer
      - .actual_access:  read_only
        .address_space:  global
        .offset:         16
        .size:           8
        .value_kind:     global_buffer
      - .actual_access:  read_only
        .address_space:  global
        .offset:         24
        .size:           8
        .value_kind:     global_buffer
      - .actual_access:  read_only
        .address_space:  global
        .offset:         32
        .size:           8
        .value_kind:     global_buffer
      - .actual_access:  write_only
        .address_space:  global
        .offset:         40
        .size:           8
        .value_kind:     global_buffer
      - .actual_access:  write_only
        .address_space:  global
        .offset:         48
        .size:           8
        .value_kind:     global_buffer
    .group_segment_fixed_size: 14112
    .kernarg_segment_align: 8
    .kernarg_segment_size: 56
    .language:       OpenCL C
    .language_version:
      - 2
      - 0
    .max_flat_workgroup_size: 256
    .name:           _Z4khidPKDF16_PKfS2_S2_S0_PDF16_Pf
    .private_segment_fixed_size: 0
    .sgpr_count:     24
    .sgpr_spill_count: 0
    .symbol:         _Z4khidPKDF16_PKfS2_S2_S0_PDF16_Pf.kd
    .uniform_work_group_size: 1
    .uses_dynamic_stack: false
    .vgpr_count:     148
    .vgpr_spill_count: 0
    .wavefront_size: 64
  - .agpr_count:     144
    .args:
      - .actual_access:  read_only
        .address_space:  global
        .offset:         0
        .size:           8
        .value_kind:     global_buffer
      - .actual_access:  read_only
        .address_space:  global
        .offset:         8
        .size:           8
        .value_kind:     global_buffer
      - .actual_access:  read_only
        .address_space:  global
        .offset:         16
        .size:           8
        .value_kind:     global_buffer
      - .actual_access:  read_only
        .address_space:  global
        .offset:         24
        .size:           8
        .value_kind:     global_buffer
      - .address_space:  global
        .offset:         32
        .size:           8
        .value_kind:     global_buffer
      - .address_space:  global
        .offset:         40
        .size:           8
        .value_kind:     global_buffer
      - .address_space:  global
        .offset:         48
        .size:           8
        .value_kind:     global_buffer
    .group_segment_fixed_size: 0
    .kernarg_segment_align: 8
    .kernarg_segment_size: 56
    .language:       OpenCL C
    .language_version:
      - 2
      - 0
    .max_flat_workgroup_size: 256
    .name:           _Z6kfinalPKDF16_PKfS2_S2_PK15HIP_vector_typeIjLj4EES2_Pf
    .private_segment_fixed_size: 0
    .sgpr_count:     41
    .sgpr_spill_count: 0
    .symbol:         _Z6kfinalPKDF16_PKfS2_S2_PK15HIP_vector_typeIjLj4EES2_Pf.kd
    .uniform_work_group_size: 1
    .uses_dynamic_stack: false
    .vgpr_count:     400
    .vgpr_spill_count: 0
    .wavefront_size: 64
  - .agpr_count:     73
    .args:
      - .actual_access:  read_only
        .address_space:  global
        .offset:         0
        .size:           8
        .value_kind:     global_buffer
      - .actual_access:  read_only
        .address_space:  global
        .offset:         8
        .size:           8
        .value_kind:     global_buffer
      - .actual_access:  read_only
        .address_space:  global
        .offset:         16
        .size:           8
        .value_kind:     global_buffer
      - .actual_access:  read_only
        .address_space:  global
        .offset:         24
        .size:           8
        .value_kind:     global_buffer
      - .address_space:  global
        .offset:         32
        .size:           8
        .value_kind:     global_buffer
      - .address_space:  global
        .offset:         40
        .size:           8
        .value_kind:     global_buffer
      - .address_space:  global
        .offset:         48
        .size:           8
        .value_kind:     global_buffer
    .group_segment_fixed_size: 0
    .kernarg_segment_align: 8
    .kernarg_segment_size: 56
    .language:       OpenCL C
    .language_version:
      - 2
      - 0
    .max_flat_workgroup_size: 512
    .name:           _Z7kfinal3PKDF16_PKfS2_S2_PK15HIP_vector_typeIjLj4EES2_Pf
    .private_segment_fixed_size: 0
    .sgpr_count:     52
    .sgpr_spill_count: 0
    .symbol:         _Z7kfinal3PKDF16_PKfS2_S2_PK15HIP_vector_typeIjLj4EES2_Pf.kd
    .uniform_work_group_size: 1
    .uses_dynamic_stack: false
    .vgpr_count:     213
    .vgpr_spill_count: 0
    .wavefront_size: 64
